# final_d + L2 software prefetch of the next unit's A row tile (quarter per workgroup) during the P8 epilogue
# speedup vs baseline: 1.0105x; 1.0105x over previous
.LBB0_1090:
	v_lshl_add_u32 v2, s27, 8, v215
	v_ashrrev_i32_e32 v3, 31, v2
	s_ashr_i32 s0, s84, 2
	s_lshl_b32 s1, s84, 8
	v_lshl_add_u64 v[4:5], v[2:3], 2, s[92:93]
	v_add_u32_e32 v6, 0x80, v2
	v_add_u32_e32 v8, 0x90, v2
	v_add_u32_e32 v10, 0xa0, v2
	v_add_u32_e32 v2, 0xb0, v2
	s_and_b32 s84, s1, 0x300
	v_ashrrev_i32_e32 v3, 31, v2
	s_ashr_i32 s1, s0, 31
	v_readlane_b32 s40, v239, 7
	s_waitcnt vmcnt(0)
	v_ashrrev_i32_e32 v7, 31, v6
	v_ashrrev_i32_e32 v9, 31, v8
	v_ashrrev_i32_e32 v11, 31, v10
	v_lshl_add_u64 v[2:3], v[2:3], 2, s[92:93]
	s_lshl_b64 s[0:1], s[0:1], 12
	v_readlane_b32 s50, v239, 17
	v_lshl_add_u64 v[6:7], v[6:7], 2, s[92:93]
	v_lshl_add_u64 v[8:9], v[8:9], 2, s[92:93]
	v_lshl_add_u64 v[10:11], v[10:11], 2, s[92:93]
	global_load_dword v34, v[4:5], off
	global_load_dword v36, v[4:5], off offset:64
	global_load_dword v38, v[4:5], off offset:128
	global_load_dword v26, v[4:5], off offset:192
	global_load_dword v24, v[6:7], off
	global_load_dword v22, v[8:9], off
	global_load_dword v20, v[10:11], off
	global_load_dword v18, v[2:3], off
	v_or_b32_e32 v2, s84, v217
	v_readlane_b32 s51, v239, 18
	s_add_u32 s0, s50, s0
	s_addc_u32 s1, s51, s1
	v_lshlrev_b32_e32 v2, 2, v2
	global_load_dwordx4 v[14:17], v2, s[0:1]
	global_load_dwordx4 v[10:13], v2, s[0:1] offset:16
	global_load_dwordx4 v[6:9], v2, s[0:1] offset:128
	s_nop 0
	global_load_dwordx4 v[2:5], v2, s[0:1] offset:144
	v_mov_b32_e32 v28, v199
	v_mov_b32_e32 v29, v199
	v_mov_b32_e32 v30, v199
	v_mov_b32_e32 v31, v199
	v_mov_b32_e32 v32, v199
	v_mov_b32_e32 v33, v199
	v_readlane_b32 s41, v239, 8
	v_readlane_b32 s42, v239, 9
	v_readlane_b32 s43, v239, 10
	v_readlane_b32 s44, v239, 11
	v_readlane_b32 s45, v239, 12
	v_readlane_b32 s46, v239, 13
	v_readlane_b32 s47, v239, 14
	v_readlane_b32 s48, v239, 15
	v_readlane_b32 s49, v239, 16
	v_readlane_b32 s52, v239, 19
	v_readlane_b32 s53, v239, 20
	v_readlane_b32 s54, v239, 21
	v_readlane_b32 s55, v239, 22
	s_waitcnt vmcnt(0)
	s_cmp_lg_u64 s[2:3], 0
	s_cbranch_scc1 .Lpf8_skip
	v_readlane_b32 s98, v239, 44
	v_readlane_b32 s99, v239, 45
	s_add_u32 s98, s98, 0x1a000000
	s_addc_u32 s99, s99, 0
	s_lshl_b32 s100, s68, 18
	s_add_u32 s98, s98, s100
	s_addc_u32 s99, s99, 0
	s_lshl_b32 s100, s84, 8
	s_add_u32 s98, s98, s100
	s_addc_u32 s99, s99, 0
	v_readlane_b32 s100, v239, 0
	s_lshr_b32 s100, s100, 6
	s_lshl_b32 s100, s100, 13
	s_add_u32 s98, s98, s100
	s_addc_u32 s99, s99, 0
	v_mbcnt_lo_u32_b32 v244, -1, 0
	v_mbcnt_hi_u32_b32 v244, -1, v244
	v_lshlrev_b32_e32 v244, 4, v244
	global_load_dwordx4 v[240:243], v244, s[98:99]
	global_load_dwordx4 v[240:243], v244, s[98:99] offset:1024
	global_load_dwordx4 v[240:243], v244, s[98:99] offset:2048
	global_load_dwordx4 v[240:243], v244, s[98:99] offset:3072
	s_add_u32 s98, s98, 0x1000
	s_addc_u32 s99, s99, 0
	global_load_dwordx4 v[240:243], v244, s[98:99]
	global_load_dwordx4 v[240:243], v244, s[98:99] offset:1024
	global_load_dwordx4 v[240:243], v244, s[98:99] offset:2048
	global_load_dwordx4 v[240:243], v244, s[98:99] offset:3072
.Lpf8_skip:
	v_ashrrev_i32_e32 v35, 31, v34
	v_lshlrev_b64 v[40:41], 10, v[34:35]
	v_cmp_lt_i64_e32 vcc, -1, v[34:35]
	v_ashrrev_i32_e32 v37, 31, v36
	v_lshlrev_b64 v[42:43], 10, v[36:37]
	v_cndmask_b32_e32 v35, 0, v41, vcc
	v_cndmask_b32_e32 v34, v221, v40, vcc
	v_cmp_lt_i64_e64 s[0:1], -1, v[36:37]
	v_lshl_add_u64 v[34:35], s[94:95], 0, v[34:35]
	v_lshl_add_u64 v[34:35], v[34:35], 0, s[84:85]
	v_pk_fma_f32 v[40:41], v[190:191], s[8:9], v[14:15] op_sel_hi:[1,0,1]
	v_pk_fma_f32 v[46:47], v[186:187], s[8:9], v[10:11] op_sel_hi:[1,0,1]
	v_pk_fma_f32 v[50:51], v[174:175], s[8:9], v[6:7] op_sel_hi:[1,0,1]
	v_pk_fma_f32 v[54:55], v[170:171], s[8:9], v[2:3] op_sel_hi:[1,0,1]
	v_cvt_pk_fp8_f32 v28, v40, v41
	v_cvt_pk_fp8_f32 v29, v46, v47
	v_cvt_pk_fp8_f32 v30, v50, v51
	v_cvt_pk_fp8_f32 v31, v54, v55
	v_pk_fma_f32 v[36:37], v[192:193], s[8:9], v[16:17] op_sel_hi:[1,0,1]
	v_pk_fma_f32 v[44:45], v[188:189], s[8:9], v[12:13] op_sel_hi:[1,0,1]
	v_pk_fma_f32 v[48:49], v[176:177], s[8:9], v[8:9] op_sel_hi:[1,0,1]
	v_pk_fma_f32 v[52:53], v[172:173], s[8:9], v[4:5] op_sel_hi:[1,0,1]
	v_cvt_pk_fp8_f32 v28, v36, v37 op_sel:[0,0,1]
	v_cvt_pk_fp8_f32 v29, v44, v45 op_sel:[0,0,1]
	v_cvt_pk_fp8_f32 v30, v48, v49 op_sel:[0,0,1]
	v_cvt_pk_fp8_f32 v31, v52, v53 op_sel:[0,0,1]
	v_lshl_add_u64 v[34:35], v[34:35], 0, s[6:7]
	v_lshl_add_u64 v[34:35], v[34:35], 0, v[202:203]
	v_permlane16_swap_b32_e32 v28, v30
	v_permlane16_swap_b32_e32 v29, v31
	v_pk_fma_f32 v[58:59], v[182:183], s[8:9], v[14:15] op_sel_hi:[1,0,1]
	v_pk_fma_f32 v[62:63], v[178:179], s[8:9], v[10:11] op_sel_hi:[1,0,1]
	global_store_dwordx4 v[34:35], v[28:31], off
	v_mov_b32_e32 v34, v199
	v_mov_b32_e32 v35, v199
	v_pk_fma_f32 v[28:29], v[166:167], s[8:9], v[6:7] op_sel_hi:[1,0,1]
	v_pk_fma_f32 v[30:31], v[162:163], s[8:9], v[2:3] op_sel_hi:[1,0,1]
	v_cvt_pk_fp8_f32 v32, v58, v59
	v_cvt_pk_fp8_f32 v33, v62, v63
	v_cvt_pk_fp8_f32 v34, v28, v29
	v_cvt_pk_fp8_f32 v35, v30, v31
	v_pk_fma_f32 v[56:57], v[184:185], s[8:9], v[16:17] op_sel_hi:[1,0,1]
	v_pk_fma_f32 v[60:61], v[180:181], s[8:9], v[12:13] op_sel_hi:[1,0,1]
	v_pk_fma_f32 v[28:29], v[168:169], s[8:9], v[8:9] op_sel_hi:[1,0,1]
	v_pk_fma_f32 v[30:31], v[164:165], s[8:9], v[4:5] op_sel_hi:[1,0,1]
	v_cndmask_b32_e64 v43, 0, v43, s[0:1]
	v_cndmask_b32_e64 v42, v221, v42, s[0:1]
	v_cvt_pk_fp8_f32 v32, v56, v57 op_sel:[0,0,1]
	v_cvt_pk_fp8_f32 v33, v60, v61 op_sel:[0,0,1]
	v_cvt_pk_fp8_f32 v34, v28, v29 op_sel:[0,0,1]
	v_cvt_pk_fp8_f32 v35, v30, v31 op_sel:[0,0,1]
	v_lshl_add_u64 v[40:41], s[94:95], 0, v[42:43]
	v_lshl_add_u64 v[40:41], v[40:41], 0, s[84:85]
	v_lshl_add_u64 v[40:41], v[40:41], 0, s[6:7]
	v_ashrrev_i32_e32 v39, 31, v38
	v_lshl_add_u64 v[28:29], v[40:41], 0, v[202:203]
	v_permlane16_swap_b32_e32 v32, v34
	v_permlane16_swap_b32_e32 v33, v35
	global_store_dwordx4 v[28:29], v[32:35], off
	v_lshlrev_b64 v[28:29], 10, v[38:39]
	v_cmp_lt_i64_e32 vcc, -1, v[38:39]
	v_pk_fma_f32 v[30:31], v[158:159], s[8:9], v[14:15] op_sel_hi:[1,0,1]
	v_pk_fma_f32 v[34:35], v[154:155], s[8:9], v[10:11] op_sel_hi:[1,0,1]
	v_cndmask_b32_e32 v29, 0, v29, vcc
	v_cndmask_b32_e32 v28, v221, v28, vcc
	v_lshl_add_u64 v[28:29], s[94:95], 0, v[28:29]
	v_lshl_add_u64 v[28:29], v[28:29], 0, s[84:85]
	v_lshl_add_u64 v[32:33], v[28:29], 0, s[6:7]
	v_mov_b32_e32 v28, v199
	v_mov_b32_e32 v29, v199
	v_cvt_pk_fp8_f32 v28, v30, v31
	v_cvt_pk_fp8_f32 v29, v34, v35
	v_pk_fma_f32 v[30:31], v[160:161], s[8:9], v[16:17] op_sel_hi:[1,0,1]
	v_pk_fma_f32 v[34:35], v[156:157], s[8:9], v[12:13] op_sel_hi:[1,0,1]
	v_cvt_pk_fp8_f32 v28, v30, v31 op_sel:[0,0,1]
	v_cvt_pk_fp8_f32 v29, v34, v35 op_sel:[0,0,1]
	v_pk_fma_f32 v[34:35], v[150:151], s[8:9], v[6:7] op_sel_hi:[1,0,1]
	v_pk_fma_f32 v[36:37], v[146:147], s[8:9], v[2:3] op_sel_hi:[1,0,1]
	v_mov_b32_e32 v30, v199
	v_mov_b32_e32 v31, v199
	v_cvt_pk_fp8_f32 v30, v34, v35
	v_cvt_pk_fp8_f32 v31, v36, v37
	v_pk_fma_f32 v[34:35], v[152:153], s[8:9], v[8:9] op_sel_hi:[1,0,1]
	v_pk_fma_f32 v[36:37], v[148:149], s[8:9], v[4:5] op_sel_hi:[1,0,1]
	v_cvt_pk_fp8_f32 v30, v34, v35 op_sel:[0,0,1]
	v_cvt_pk_fp8_f32 v31, v36, v37 op_sel:[0,0,1]
	v_ashrrev_i32_e32 v27, 31, v26
	v_lshl_add_u64 v[32:33], v[32:33], 0, v[202:203]
	v_permlane16_swap_b32_e32 v28, v30
	v_permlane16_swap_b32_e32 v29, v31
	global_store_dwordx4 v[32:33], v[28:31], off
	v_cmp_lt_i64_e32 vcc, -1, v[26:27]
	v_pk_fma_f32 v[32:33], v[138:139], s[8:9], v[10:11] op_sel_hi:[1,0,1]
	v_lshlrev_b64 v[28:29], 10, v[26:27]
	v_cndmask_b32_e32 v27, 0, v29, vcc
	v_cndmask_b32_e32 v26, v221, v28, vcc
	v_lshl_add_u64 v[26:27], s[94:95], 0, v[26:27]
	v_lshl_add_u64 v[26:27], v[26:27], 0, s[84:85]
	v_lshl_add_u64 v[30:31], v[26:27], 0, s[6:7]
	v_pk_fma_f32 v[28:29], v[142:143], s[8:9], v[14:15] op_sel_hi:[1,0,1]
	v_mov_b32_e32 v26, v199
	v_mov_b32_e32 v27, v199
	v_cvt_pk_fp8_f32 v26, v28, v29
	v_cvt_pk_fp8_f32 v27, v32, v33
	v_pk_fma_f32 v[28:29], v[144:145], s[8:9], v[16:17] op_sel_hi:[1,0,1]
	v_pk_fma_f32 v[32:33], v[140:141], s[8:9], v[12:13] op_sel_hi:[1,0,1]
	v_cvt_pk_fp8_f32 v26, v28, v29 op_sel:[0,0,1]
	v_cvt_pk_fp8_f32 v27, v32, v33 op_sel:[0,0,1]
	v_pk_fma_f32 v[32:33], v[134:135], s[8:9], v[6:7] op_sel_hi:[1,0,1]
	v_pk_fma_f32 v[34:35], v[130:131], s[8:9], v[2:3] op_sel_hi:[1,0,1]
	v_mov_b32_e32 v28, v199
	v_mov_b32_e32 v29, v199
	v_cvt_pk_fp8_f32 v28, v32, v33
	v_cvt_pk_fp8_f32 v29, v34, v35
	v_pk_fma_f32 v[32:33], v[136:137], s[8:9], v[8:9] op_sel_hi:[1,0,1]
	v_pk_fma_f32 v[34:35], v[132:133], s[8:9], v[4:5] op_sel_hi:[1,0,1]
	v_cvt_pk_fp8_f32 v28, v32, v33 op_sel:[0,0,1]
	v_cvt_pk_fp8_f32 v29, v34, v35 op_sel:[0,0,1]
	v_ashrrev_i32_e32 v25, 31, v24
	v_lshl_add_u64 v[30:31], v[30:31], 0, v[202:203]
	v_permlane16_swap_b32_e32 v26, v28
	v_permlane16_swap_b32_e32 v27, v29
	global_store_dwordx4 v[30:31], v[26:29], off
	v_cmp_lt_i64_e32 vcc, -1, v[24:25]
	v_pk_fma_f32 v[30:31], v[122:123], s[8:9], v[10:11] op_sel_hi:[1,0,1]
	v_lshlrev_b64 v[26:27], 10, v[24:25]
	v_cndmask_b32_e32 v25, 0, v27, vcc
	v_cndmask_b32_e32 v24, v221, v26, vcc
	v_lshl_add_u64 v[24:25], s[94:95], 0, v[24:25]
	v_lshl_add_u64 v[24:25], v[24:25], 0, s[84:85]
	v_lshl_add_u64 v[28:29], v[24:25], 0, s[6:7]
	v_pk_fma_f32 v[26:27], v[126:127], s[8:9], v[14:15] op_sel_hi:[1,0,1]
	v_mov_b32_e32 v24, v199
	v_mov_b32_e32 v25, v199
	v_cvt_pk_fp8_f32 v24, v26, v27
	v_cvt_pk_fp8_f32 v25, v30, v31
	v_pk_fma_f32 v[26:27], v[128:129], s[8:9], v[16:17] op_sel_hi:[1,0,1]
	v_pk_fma_f32 v[30:31], v[124:125], s[8:9], v[12:13] op_sel_hi:[1,0,1]
	v_cvt_pk_fp8_f32 v24, v26, v27 op_sel:[0,0,1]
	v_cvt_pk_fp8_f32 v25, v30, v31 op_sel:[0,0,1]
	v_pk_fma_f32 v[30:31], v[118:119], s[8:9], v[6:7] op_sel_hi:[1,0,1]
	v_pk_fma_f32 v[32:33], v[114:115], s[8:9], v[2:3] op_sel_hi:[1,0,1]
	v_mov_b32_e32 v26, v199
	v_mov_b32_e32 v27, v199
	v_cvt_pk_fp8_f32 v26, v30, v31
	v_cvt_pk_fp8_f32 v27, v32, v33
	v_pk_fma_f32 v[30:31], v[120:121], s[8:9], v[8:9] op_sel_hi:[1,0,1]
	v_pk_fma_f32 v[32:33], v[116:117], s[8:9], v[4:5] op_sel_hi:[1,0,1]
	v_cvt_pk_fp8_f32 v26, v30, v31 op_sel:[0,0,1]
	v_cvt_pk_fp8_f32 v27, v32, v33 op_sel:[0,0,1]
	v_ashrrev_i32_e32 v23, 31, v22
	v_lshl_add_u64 v[28:29], v[28:29], 0, v[202:203]
	v_permlane16_swap_b32_e32 v24, v26
	v_permlane16_swap_b32_e32 v25, v27
	global_store_dwordx4 v[28:29], v[24:27], off
	v_cmp_lt_i64_e32 vcc, -1, v[22:23]
	v_pk_fma_f32 v[28:29], v[98:99], s[8:9], v[10:11] op_sel_hi:[1,0,1]
	v_lshlrev_b64 v[24:25], 10, v[22:23]
	v_cndmask_b32_e32 v23, 0, v25, vcc
	v_cndmask_b32_e32 v22, v221, v24, vcc
	v_lshl_add_u64 v[22:23], s[94:95], 0, v[22:23]
	v_lshl_add_u64 v[22:23], v[22:23], 0, s[84:85]
	v_lshl_add_u64 v[26:27], v[22:23], 0, s[6:7]
	v_pk_fma_f32 v[24:25], v[106:107], s[8:9], v[14:15] op_sel_hi:[1,0,1]
	v_mov_b32_e32 v22, v199
	v_mov_b32_e32 v23, v199
	v_cvt_pk_fp8_f32 v22, v24, v25
	v_cvt_pk_fp8_f32 v23, v28, v29
	v_pk_fma_f32 v[24:25], v[108:109], s[8:9], v[16:17] op_sel_hi:[1,0,1]
	v_pk_fma_f32 v[28:29], v[100:101], s[8:9], v[12:13] op_sel_hi:[1,0,1]
	v_cvt_pk_fp8_f32 v22, v24, v25 op_sel:[0,0,1]
	v_cvt_pk_fp8_f32 v23, v28, v29 op_sel:[0,0,1]
	v_pk_fma_f32 v[28:29], v[90:91], s[8:9], v[6:7] op_sel_hi:[1,0,1]
	v_pk_fma_f32 v[30:31], v[82:83], s[8:9], v[2:3] op_sel_hi:[1,0,1]
	v_mov_b32_e32 v24, v199
	v_mov_b32_e32 v25, v199
	v_cvt_pk_fp8_f32 v24, v28, v29
	v_cvt_pk_fp8_f32 v25, v30, v31
	v_pk_fma_f32 v[28:29], v[92:93], s[8:9], v[8:9] op_sel_hi:[1,0,1]
	v_pk_fma_f32 v[30:31], v[84:85], s[8:9], v[4:5] op_sel_hi:[1,0,1]
	v_cvt_pk_fp8_f32 v24, v28, v29 op_sel:[0,0,1]
	v_cvt_pk_fp8_f32 v25, v30, v31 op_sel:[0,0,1]
	v_ashrrev_i32_e32 v21, 31, v20
	v_lshl_add_u64 v[26:27], v[26:27], 0, v[202:203]
	v_permlane16_swap_b32_e32 v22, v24
	v_permlane16_swap_b32_e32 v23, v25
	global_store_dwordx4 v[26:27], v[22:25], off
	v_cmp_lt_i64_e32 vcc, -1, v[20:21]
	v_pk_fma_f32 v[26:27], v[74:75], s[8:9], v[10:11] op_sel_hi:[1,0,1]
	v_lshlrev_b64 v[22:23], 10, v[20:21]
	v_cndmask_b32_e32 v21, 0, v23, vcc
	v_cndmask_b32_e32 v20, v221, v22, vcc
	v_lshl_add_u64 v[20:21], s[94:95], 0, v[20:21]
	v_lshl_add_u64 v[20:21], v[20:21], 0, s[84:85]
	v_lshl_add_u64 v[24:25], v[20:21], 0, s[6:7]
	v_pk_fma_f32 v[22:23], v[78:79], s[8:9], v[14:15] op_sel_hi:[1,0,1]
	v_mov_b32_e32 v20, v199
	v_mov_b32_e32 v21, v199
	v_cvt_pk_fp8_f32 v20, v22, v23
	v_cvt_pk_fp8_f32 v21, v26, v27
	v_pk_fma_f32 v[22:23], v[80:81], s[8:9], v[16:17] op_sel_hi:[1,0,1]
	v_pk_fma_f32 v[26:27], v[76:77], s[8:9], v[12:13] op_sel_hi:[1,0,1]
	v_cvt_pk_fp8_f32 v20, v22, v23 op_sel:[0,0,1]
	v_cvt_pk_fp8_f32 v21, v26, v27 op_sel:[0,0,1]
	v_pk_fma_f32 v[26:27], v[102:103], s[8:9], v[6:7] op_sel_hi:[1,0,1]
	v_pk_fma_f32 v[28:29], v[110:111], s[8:9], v[2:3] op_sel_hi:[1,0,1]
	v_mov_b32_e32 v22, v199
	v_mov_b32_e32 v23, v199
	v_cvt_pk_fp8_f32 v22, v26, v27
	v_cvt_pk_fp8_f32 v23, v28, v29
	v_pk_fma_f32 v[26:27], v[104:105], s[8:9], v[8:9] op_sel_hi:[1,0,1]
	v_pk_fma_f32 v[28:29], v[112:113], s[8:9], v[4:5] op_sel_hi:[1,0,1]
	v_cvt_pk_fp8_f32 v22, v26, v27 op_sel:[0,0,1]
	v_cvt_pk_fp8_f32 v23, v28, v29 op_sel:[0,0,1]
	v_ashrrev_i32_e32 v19, 31, v18
	v_lshl_add_u64 v[24:25], v[24:25], 0, v[202:203]
	v_permlane16_swap_b32_e32 v20, v22
	v_permlane16_swap_b32_e32 v21, v23
	global_store_dwordx4 v[24:25], v[20:23], off
	v_cmp_lt_i64_e32 vcc, -1, v[18:19]
	v_pk_fma_f32 v[12:13], v[68:69], s[8:9], v[12:13] op_sel_hi:[1,0,1]
	v_lshlrev_b64 v[20:21], 10, v[18:19]
	v_cndmask_b32_e32 v19, 0, v21, vcc
	v_cndmask_b32_e32 v18, v221, v20, vcc
	v_pk_fma_f32 v[20:21], v[66:67], s[8:9], v[10:11] op_sel_hi:[1,0,1]
	v_mov_b32_e32 v11, v199
	v_cvt_pk_fp8_f32 v11, v20, v21
	v_pk_fma_f32 v[14:15], v[70:71], s[8:9], v[14:15] op_sel_hi:[1,0,1]
	v_mov_b32_e32 v10, v199
	v_pk_fma_f32 v[6:7], v[86:87], s[8:9], v[6:7] op_sel_hi:[1,0,1]
	v_cvt_pk_fp8_f32 v11, v12, v13 op_sel:[0,0,1]
	v_pk_fma_f32 v[2:3], v[94:95], s[8:9], v[2:3] op_sel_hi:[1,0,1]
	v_mov_b32_e32 v12, v199
	v_mov_b32_e32 v13, v199
	v_cvt_pk_fp8_f32 v10, v14, v15
	v_cvt_pk_fp8_f32 v12, v6, v7
	v_cvt_pk_fp8_f32 v13, v2, v3
	v_pk_fma_f32 v[14:15], v[72:73], s[8:9], v[16:17] op_sel_hi:[1,0,1]
	v_pk_fma_f32 v[2:3], v[88:89], s[8:9], v[8:9] op_sel_hi:[1,0,1]
	v_pk_fma_f32 v[4:5], v[96:97], s[8:9], v[4:5] op_sel_hi:[1,0,1]
	v_cvt_pk_fp8_f32 v10, v14, v15 op_sel:[0,0,1]
	v_cvt_pk_fp8_f32 v12, v2, v3 op_sel:[0,0,1]
	v_cvt_pk_fp8_f32 v13, v4, v5 op_sel:[0,0,1]
	v_lshl_add_u64 v[18:19], s[94:95], 0, v[18:19]
	v_lshl_add_u64 v[18:19], v[18:19], 0, s[84:85]
	v_lshl_add_u64 v[18:19], v[18:19], 0, s[6:7]
	v_lshl_add_u64 v[2:3], v[18:19], 0, v[202:203]
	v_permlane16_swap_b32_e32 v10, v12
	v_permlane16_swap_b32_e32 v11, v13
	s_and_b64 vcc, exec, s[2:3]
	s_mov_b64 s[0:1], -1
	global_store_dwordx4 v[2:3], v[10:13], off
	s_cbranch_vccnz .LBB0_1076
	s_andn2_b64 vcc, exec, s[90:91]
	s_cbranch_vccnz .LBB0_1075
	s_barrier
	s_branch .LBB0_1075
